# attention: relative-position bias via clip-padded LDS table copy, one ds_read per score (on top of exp fma fold and bonus-scalar handoff)
# speedup vs baseline: 1.0131x; 1.0049x over previous
; #define GAS __attribute__((address_space(1)))
; #define AT_STAGE_LOAD(kc_) do { kreg = *(const GAS v4u*)(PROJ + ((size_t)b * SEQ + (size_t)(kc_) * 64 + srow) * PROJ_LD + PJ_K + h * 64 + spc * 8); \
;                                 vreg = *(const GAS v4u*)(VT + (size_t)(h * 64 + srow) * T + (size_t)b * SEQ + (size_t)(kc_) * 64 + spc * 8); } while (0)
; #define AT_STAGE_WRITE(buf_) do { *(LAS v4u*)(F.lds + A_KOFF + (buf_) * AKV + srow * 144 + spc * 16) = kreg; *(LAS v4u*)(F.lds + A_VOFF + (buf_) * AKV + srow * 144 + spc * 16) = vreg; } while (0)
; __device__ __forceinline__ void p2_shift_attn(Frame& F0, const In& I) {
;     ...
;     for (int task = F.vcu; task < BATCH * AH * (SEQ / 256); task += F.G) {
;         const int bh = task >> 5, q256 = task & 31, b = bh >> 4, h = bh & 15, c0 = q256 * 4;
;         const int q0 = q256 * 256 + F.wave * 32, cw = c0 + (F.wave >> 1);
;         const int kc_lo = (c0 > LEFT) ? c0 - LEFT : 0, kc_hi = c0 + 3;
;         __syncthreads();
;         if (F.tid < REL_TABLE) tbl[F.tid] = I.rel_bias[h * REL_TABLE + F.tid];
;         const size_t tokq = (size_t)b * SEQ + q0 + r;
;         bf16x8 qf[4];
; #pragma unroll
;         for (int s = 0; s < 4; ++s) qf[s] = *(const GAS bf16x8*)(PROJ + tokq * PROJ_LD + PJ_Q + h * 64 + 16 * s + 8 * hh);
;         f32x16 o0, o1;
; #pragma unroll
;         for (int i = 0; i < 16; ++i) { o0[i] = 0.f; o1[i] = 0.f; }
;         float m_run = -1e30f, l_run = 0.f;
;         v4u kreg, vreg;
;     ...
;         AT_STAGE_LOAD(kc_lo); AT_STAGE_WRITE(0);
;         __syncthreads();
.LBB0_876:
	s_bfe_u32 s16, s26, 0x40005
	s_barrier
	s_and_saveexec_b64 s[12:13], s[2:3]
	s_cbranch_execz .LBB0_878
	s_mul_i32 s8, s16, 0x140
	v_add_u32_e32 v4, s8, v1
	v_readlane_b32 s36, v254, 5
	v_ashrrev_i32_e32 v5, 31, v4
	v_readlane_b32 s40, v254, 9
	v_readlane_b32 s41, v254, 10
	v_readlane_b32 s37, v254, 6
	v_readlane_b32 s38, v254, 7
	v_lshl_add_u64 v[4:5], v[4:5], 2, s[40:41]
	global_load_dword v3, v[4:5], off
	v_readlane_b32 s39, v254, 8
	v_readlane_b32 s42, v254, 11
	v_readlane_b32 s43, v254, 12
	v_readlane_b32 s44, v254, 13
	v_readlane_b32 s45, v254, 14
	v_readlane_b32 s46, v254, 15
	v_readlane_b32 s47, v254, 16
	v_readlane_b32 s48, v254, 17
	v_readlane_b32 s49, v254, 18
	v_readlane_b32 s50, v254, 19
	v_readlane_b32 s51, v254, 20
	s_waitcnt vmcnt(0)
	ds_write_b32 v125, v3
	ds_write_b32 v125, v3 offset:40960
.LBB0_878:
	s_or_b64 exec, exec, s[12:13]
	v_readlane_b32 s100, v254, 9
	v_readlane_b32 s101, v254, 10
	s_mul_i32 s98, s16, 0x140
	s_add_i32 s98, s98, 319
	s_lshl_b32 s98, s98, 2
	s_nop 4
	s_load_dword s99, s[100:101], s98
	s_waitcnt lgkmcnt(0)
	v_mov_b32_e32 v177, s99
	ds_write_b32 v125, v177 offset:42240
	s_and_b32 s8, s26, 31
	s_lshl_b32 s28, s8, 2
	s_lshl_b32 s12, s8, 8
	s_ashr_i32 s14, s26, 9
	s_add_i32 s13, s12, s20
	s_add_i32 s12, s28, -8
	s_cmp_gt_u32 s8, 2
	s_cselect_b32 s12, s12, 0
	s_ashr_i32 s15, s14, 31
	s_or_b32 s27, s28, 3
	s_lshl_b64 s[18:19], s[14:15], 13
	s_ashr_i32 s8, s13, 31
	s_add_u32 s13, s18, s13
	v_or_b32_e32 v140, s13, v124
	s_addc_u32 s29, s19, s8
	v_mad_u64_u32 v[4:5], s[30:31], v140, s23, v[134:135]
	s_ashr_i32 s13, s12, 31
	s_lshl_b32 s8, s16, 6
	s_lshl_b32 s16, s16, 7
	s_lshl_b64 s[30:31], s[12:13], 6
	s_add_u32 s18, s30, s18
	s_addc_u32 s19, s31, s19
	v_lshl_add_u64 v[6:7], s[18:19], 0, v[126:127]
	v_mad_u64_u32 v[8:9], s[18:19], v6, s23, v[134:135]
	s_mov_b32 s17, s9
	v_mad_i32_i24 v9, v7, s23, v9
	v_lshl_add_u64 v[6:7], v[8:9], 0, s[16:17]
	v_add_u32_e32 v8, s8, v126
	v_ashrrev_i32_e32 v9, 31, v8
	v_mad_i32_i24 v5, s29, v167, v5
	v_lshlrev_b64 v[8:9], 16, v[8:9]
	v_lshl_add_u64 v[4:5], v[4:5], 0, s[16:17]
	v_lshl_add_u64 v[8:9], s[0:1], 0, v[8:9]
	s_lshl_b64 s[16:17], s[14:15], 14
	v_lshl_add_u64 v[8:9], v[8:9], 0, s[16:17]
	s_lshl_b64 s[18:19], s[12:13], 7
	v_lshl_add_u64 v[6:7], v[6:7], 0, v[138:139]
	v_lshl_add_u64 v[8:9], v[8:9], 0, s[18:19]
	v_lshl_add_u64 v[4:5], v[4:5], 0, v[136:137]
	v_lshl_add_u64 v[8:9], v[8:9], 0, v[138:139]
	global_load_dwordx4 v[68:71], v[6:7], off offset:2048
	global_load_dwordx4 v[80:83], v[8:9], off
	global_load_dwordx4 v[72:75], v[4:5], off
	global_load_dwordx4 v[76:79], v[4:5], off offset:32
	global_load_dwordx4 v[84:87], v[4:5], off offset:64
	global_load_dwordx4 v[88:91], v[4:5], off offset:96
	v_mov_b32_e32 v141, s29
	s_cmp_gt_i32 s12, s27
	s_waitcnt vmcnt(5)
	ds_write_b128 v162, v[68:71] offset:2048
	s_waitcnt vmcnt(4)
	ds_write_b128 v162, v[80:83] offset:20480
	s_waitcnt lgkmcnt(0)
	s_barrier
	s_cbranch_scc1 .LBB0_874
	s_lshr_b32 s13, s26, 5
	s_and_b32 s15, s25, 31
	s_lshl_b32 s15, s15, 8
	s_and_b32 s13, s13, 15
	v_lshl_add_u32 v4, s13, 6, v126
	s_lshl_b32 s30, s13, 7
	s_add_i32 s13, s28, s21
	s_add_i32 s15, s22, s15
	s_lshl_b32 s29, s12, 6
	s_add_i32 s28, s13, -8
	s_sub_i32 s29, s15, s29
	v_ashrrev_i32_e32 v5, 31, v4
	s_add_u32 s16, s18, s16
	v_lshlrev_b64 v[4:5], 16, v[4:5]
	s_addc_u32 s17, s19, s17
	v_lshl_add_u64 v[4:5], s[16:17], 0, v[4:5]
	s_mul_hi_i32 s15, s14, 0x2100000
	s_mul_i32 s14, s14, 0x2100000
	s_mul_i32 s17, s12, 0x42000
	v_mov_b32_e32 v16, v2
	v_mov_b32_e32 v17, v2
	v_lshl_add_u64 v[142:143], v[130:131], 0, v[4:5]
	s_mul_hi_i32 s16, s12, 0x42000
	s_add_u32 s14, s14, s17
	v_mov_b32_e32 v3, v2
	v_mov_b32_e32 v4, v2
	v_mov_b32_e32 v5, v2
	v_mov_b32_e32 v6, v2
	v_mov_b32_e32 v7, v2
	v_mov_b32_e32 v8, v2
	v_mov_b32_e32 v9, v2
	v_mov_b32_e32 v10, v2
	v_mov_b32_e32 v11, v2
	v_mov_b32_e32 v12, v2
	v_mov_b32_e32 v13, v2
	v_mov_b32_e32 v14, v2
	v_mov_b32_e32 v15, v2
	v_mov_b64_e32 v[34:35], v[16:17]
	s_addc_u32 s15, s15, s16
	s_or_b32 s14, s14, s30
	v_mov_b64_e32 v[32:33], v[14:15]
	v_mov_b64_e32 v[30:31], v[12:13]
	v_mov_b64_e32 v[28:29], v[10:11]
	v_mov_b64_e32 v[26:27], v[8:9]
	v_mov_b64_e32 v[24:25], v[6:7]
	v_mov_b64_e32 v[22:23], v[4:5]
	v_mov_b64_e32 v[20:21], v[2:3]
	v_mov_b64_e32 v[18:19], v[16:17]
	v_lshl_add_u64 v[144:145], v[132:133], 0, s[14:15]
	v_mov_b32_e32 v168, 0
	v_mov_b32_e32 v169, 0xf149f2ca
	v_mov_b64_e32 v[16:17], v[14:15]
	v_mov_b64_e32 v[14:15], v[12:13]
	v_mov_b64_e32 v[12:13], v[10:11]
	v_mov_b64_e32 v[10:11], v[8:9]
	v_mov_b64_e32 v[8:9], v[6:7]
	v_mov_b64_e32 v[6:7], v[4:5]
	v_mov_b64_e32 v[4:5], v[2:3]

; #define LAS __attribute__((address_space(3)))
; __device__ __forceinline__ void p2_shift_attn(Frame& F0, const In& I) {
;     ...
;         for (int kc = kc_lo; kc <= kc_hi; ++kc) {
;             const int buf = (kc - kc_lo) & 1;
;             if (kc < kc_hi) AT_STAGE_LOAD(kc + 1);
;             if (kc >= cw - LEFT && kc <= cw) {
;                 const LAS unsigned char* Kb = F.lds + A_KOFF + buf * AKV; const LAS unsigned char* Vb = F.lds + A_VOFF + buf * AKV;
;                 bf16x8 kf[2][4];
; #pragma unroll
;                 for (int tt = 0; tt < 2; ++tt)
; #pragma unroll
;                     for (int s = 0; s < 4; ++s) kf[tt][s] = *(const LAS bf16x8*)(Kb + (32 * tt + rp) * 144 + 32 * s + 16 * hh);
;                 f32x16 st[2];
; #pragma unroll
;                 for (int tt = 0; tt < 2; ++tt)
; #pragma unroll
;                     for (int i = 0; i < 16; ++i) st[tt][i] = 0.f;
; #pragma unroll
;                 for (int s = 0; s < 4; ++s) { st[0] = __builtin_amdgcn_mfma_f32_32x32x16_bf16(kf[0][s], qf[s], st[0], 0, 0, 0); st[1] = __builtin_amdgcn_mfma_f32_32x32x16_bf16(kf[1][s], qf[s], st[1], 0, 0, 0); }
;                 bf16x8 va[2][2], vb[2][2];
; #pragma unroll
;                 for (int tt = 0; tt < 2; ++tt)
; #pragma unroll
;                     for (int s2 = 0; s2 < 2; ++s2) { va[tt][s2] = *(const LAS bf16x8*)(Vb + r * 144 + 64 * tt + 32 * s2 + 16 * hh); vb[tt][s2] = *(const LAS bf16x8*)(Vb + (32 + r) * 144 + 64 * tt + 32 * s2 + 16 * hh); }
;                 float mx = -1e30f;
; #pragma unroll
;                 for (int tt = 0; tt < 2; ++tt) {
;                     const int kpos0 = kc * 64 + 32 * tt;
;                     const int dbase = (q0 + r) - (kpos0 + 8 * hh);
;                     if (q0 - (kpos0 + 31) >= MAX_PAST) {
;                         const float bc = tbl[MAX_PAST + 63];
; #pragma unroll
;                         for (int i = 0; i < 16; ++i) { st[tt][i] += bc; mx = fmaxf(mx, st[tt][i]); }
;                     } else {
; #pragma unroll
;                         for (int i = 0; i < 16; ++i) { int d = dbase - (16 * (i >> 3) + 4 * ((i >> 2) & 1) + (i & 3)); d = d < MAX_PAST ? d : MAX_PAST; st[tt][i] += tbl[d + 63]; mx = fmaxf(mx, st[tt][i]); }
.LBB0_882:
	s_and_b32 s30, s12, 1
	s_cmp_lt_i32 s12, s28
	s_cselect_b64 s[18:19], -1, 0
	s_cmp_gt_i32 s12, s13
	s_cselect_b64 s[34:35], -1, 0
	s_or_b64 s[18:19], s[18:19], s[34:35]
	s_and_b64 vcc, exec, s[18:19]
	s_cbranch_vccnz .LBB0_885
	s_mul_i32 s18, s30, 0x2400
	v_add_u32_e32 v3, s18, v164
	ds_read_b128 v[36:39], v3 offset:6656
	ds_read_b128 v[52:55], v3 offset:6688
	s_add_i32 s31, s29, 32
	s_cmpk_gt_i32 s31, 0xff
	s_waitcnt vmcnt(3) lgkmcnt(1)
	v_mfma_f32_32x32x16_bf16 v[36:51], v[36:39], v[72:75], 0
	s_waitcnt vmcnt(2) lgkmcnt(0)
	v_mfma_f32_32x32x16_bf16 v[36:51], v[52:55], v[76:79], v[36:51]
	ds_read_b128 v[52:55], v3 offset:6720
	ds_read_b128 v[56:59], v3 offset:6752
	s_waitcnt vmcnt(1) lgkmcnt(1)
	v_mfma_f32_32x32x16_bf16 v[36:51], v[52:55], v[84:87], v[36:51]
	ds_read_b128 v[52:55], v3 offset:2048
	ds_read_b128 v[92:95], v3 offset:2080
	s_waitcnt vmcnt(0) lgkmcnt(2)
	v_mfma_f32_32x32x16_bf16 v[36:51], v[56:59], v[88:91], v[36:51]
	s_waitcnt lgkmcnt(1)
	v_mfma_f32_32x32x16_bf16 v[52:67], v[52:55], v[72:75], 0
	s_waitcnt lgkmcnt(0)
	v_mfma_f32_32x32x16_bf16 v[52:67], v[92:95], v[76:79], v[52:67]
	ds_read_b128 v[92:95], v3 offset:2112
	ds_read_b128 v[172:175], v3 offset:2144
	v_add_u32_e32 v3, s18, v165
	ds_read_b128 v[120:123], v3 offset:20480
	ds_read_b128 v[112:115], v3 offset:20512
	ds_read_b128 v[116:119], v3 offset:25088
	ds_read_b128 v[108:111], v3 offset:25120
	s_mov_b64 s[18:19], -1
	s_waitcnt lgkmcnt(5)
	v_mfma_f32_32x32x16_bf16 v[52:67], v[92:95], v[84:87], v[52:67]
	ds_read_b128 v[104:107], v3 offset:20544
	ds_read_b128 v[96:99], v3 offset:20576
	ds_read_b128 v[100:103], v3 offset:25152
	ds_read_b128 v[92:95], v3 offset:25184
	v_add_u32_e32 v3, s29, v166
	v_add_u32_e32 v178, 0x80, v3
	v_lshlrev_b32_e32 v178, 2, v178
	s_waitcnt lgkmcnt(8)
	v_mfma_f32_32x32x16_bf16 v[52:67], v[172:175], v[88:91], v[52:67]
	s_cbranch_scc1 .LBB0_889
	ds_read_b32 v146, v178 offset:40952
	ds_read_b32 v147, v178 offset:40948
	ds_read_b32 v148, v178 offset:40944
	ds_read_b32 v149, v178 offset:40940
	ds_read_b32 v154, v178 offset:40936
	ds_read_b32 v155, v178 offset:40932
	ds_read_b32 v156, v178 offset:40928
	ds_read_b32 v157, v178 offset:40924
	s_waitcnt lgkmcnt(6)
	v_pk_add_f32 v[152:153], v[52:53], v[146:147]
	s_waitcnt lgkmcnt(4)
	v_pk_add_f32 v[150:151], v[54:55], v[148:149]
	v_max3_f32 v146, v152, s24, v153
	v_max3_f32 v148, v146, v150, v151
	s_waitcnt lgkmcnt(2)
	v_pk_add_f32 v[146:147], v[56:57], v[154:155]
	v_max3_f32 v154, v148, v146, v147
	s_waitcnt lgkmcnt(0)
	v_pk_add_f32 v[148:149], v[58:59], v[156:157]
	v_max3_f32 v160, v154, v148, v149
	ds_read_b32 v154, v178 offset:40888
	ds_read_b32 v155, v178 offset:40884
	ds_read_b32 v156, v178 offset:40880
	ds_read_b32 v157, v178 offset:40876
	ds_read_b32 v170, v178 offset:40872
	ds_read_b32 v171, v178 offset:40868
	ds_read_b32 v172, v178 offset:40864
	ds_read_b32 v173, v178 offset:40860
	s_waitcnt lgkmcnt(6)
	v_pk_add_f32 v[158:159], v[60:61], v[154:155]
	s_nop 0
	v_max3_f32 v154, v160, v158, v159
	s_waitcnt lgkmcnt(4)
	v_pk_add_f32 v[160:161], v[62:63], v[156:157]
	s_nop 0
	v_max3_f32 v156, v154, v160, v161
	s_waitcnt lgkmcnt(2)
	v_pk_add_f32 v[154:155], v[64:65], v[170:171]
	s_nop 0
	v_max3_f32 v170, v156, v154, v155
	s_waitcnt lgkmcnt(0)
	v_pk_add_f32 v[156:157], v[66:67], v[172:173]
	s_nop 0
	v_max3_f32 v170, v170, v156, v157
	s_cbranch_execnz .LBB0_891
	s_branch .LBB0_890

; __device__ __forceinline__ void p2_shift_attn(Frame& F0, const In& I) {
;     ...
;                     const int kpos0 = kc * 64 + 32 * tt;
;                     const int dbase = (q0 + r) - (kpos0 + 8 * hh);
;                     if (q0 - (kpos0 + 31) >= MAX_PAST) {
;                         const float bc = tbl[MAX_PAST + 63];
; #pragma unroll
;                         for (int i = 0; i < 16; ++i) { st[tt][i] += bc; mx = fmaxf(mx, st[tt][i]); }
;                     } else {
; #pragma unroll
;                         for (int i = 0; i < 16; ++i) { int d = dbase - (16 * (i >> 3) + 4 * ((i >> 2) & 1) + (i & 3)); d = d < MAX_PAST ? d : MAX_PAST; st[tt][i] += tbl[d + 63]; mx = fmaxf(mx, st[tt][i]); }
;                     }
;                 }
.LBB0_891:
	s_cmpk_gt_i32 s29, 0xff
	s_mov_b64 s[18:19], -1
	s_cbranch_scc1 .LBB0_893
	s_nop 5
	ds_read_b32 v52, v178 offset:40824
	ds_read_b32 v53, v178 offset:40820
	ds_read_b32 v54, v178 offset:40816
	ds_read_b32 v55, v178 offset:40812
	ds_read_b32 v56, v178 offset:40808
	ds_read_b32 v57, v178 offset:40804
	ds_read_b32 v58, v178 offset:40800
	ds_read_b32 v59, v178 offset:40796
	s_waitcnt lgkmcnt(6)
	v_pk_add_f32 v[62:63], v[36:37], v[52:53]
	s_waitcnt lgkmcnt(4)
	v_pk_add_f32 v[60:61], v[38:39], v[54:55]
	v_max3_f32 v52, v170, v62, v63
	v_max3_f32 v52, v52, v60, v61
	s_waitcnt lgkmcnt(2)
	v_pk_add_f32 v[56:57], v[40:41], v[56:57]
	s_waitcnt lgkmcnt(0)
	v_pk_add_f32 v[58:59], v[42:43], v[58:59]
	v_max3_f32 v52, v52, v56, v57
	v_max3_f32 v64, v52, v58, v59
	ds_read_b32 v52, v178 offset:40760
	ds_read_b32 v53, v178 offset:40756
	ds_read_b32 v54, v178 offset:40752
	ds_read_b32 v55, v178 offset:40748
	ds_read_b32 v172, v178 offset:40744
	ds_read_b32 v173, v178 offset:40740
	ds_read_b32 v174, v178 offset:40736
	ds_read_b32 v175, v178 offset:40732
	s_waitcnt lgkmcnt(6)
	v_pk_add_f32 v[66:67], v[44:45], v[52:53]
	s_nop 0
	v_max3_f32 v3, v64, v66, v67
	s_waitcnt lgkmcnt(4)
	v_pk_add_f32 v[64:65], v[46:47], v[54:55]
	s_waitcnt lgkmcnt(2)
	v_pk_add_f32 v[52:53], v[48:49], v[172:173]
	v_max3_f32 v3, v3, v64, v65
	v_max3_f32 v3, v3, v52, v53
	s_waitcnt lgkmcnt(0)
	v_pk_add_f32 v[54:55], v[50:51], v[174:175]
	s_nop 0
	v_max3_f32 v171, v3, v54, v55
	s_cbranch_execz .LBB0_894
	s_branch .LBB0_895
